# baseline (speedup 1.0000x reference)
_Z8dog_mainPKfS0_S0_S0_S0_S0_S0_Pf:
	s_load_dwordx8 s[12:19], s[0:1], 0x0
	s_load_dwordx8 s[20:27], s[0:1], 0x20
	s_and_b32 s3, s2, 7
	s_lshl_b32 s3, s3, 5
	s_lshr_b32 s4, s2, 3
	s_add_i32 s4, s3, s4
	s_lshl_b32 s8, s4, 18
	v_and_b32_e32 v1, 63, v0
	v_lshrrev_b32_e32 v2, 6, v0
	v_and_b32_e32 v7, 31, v0
	v_lshlrev_b32_e32 v6, 4, v1
	v_lshl_or_b32 v5, v2, 5, v7
	v_lshl_or_b32 v6, v2, 12, v6
	v_lshlrev_b32_e32 v5, 2, v5
	s_waitcnt lgkmcnt(0)
	s_add_u32 s12, s12, s8
	s_addc_u32 s13, s13, 0
	global_load_dword v32, v5, s[18:19]
	global_load_dword v33, v5, s[20:21]
	global_load_dword v34, v5, s[22:23]
	global_load_dword v35, v5, s[24:25]
	global_load_dword v36, v5, s[14:15]
	global_load_dword v37, v5, s[16:17]
	global_load_dwordx4 v[128:131], v6, s[12:13] offset:0 nt
	global_load_dwordx4 v[132:135], v6, s[12:13] offset:1024 nt
	global_load_dwordx4 v[136:139], v6, s[12:13] offset:2048 nt
	global_load_dwordx4 v[140:143], v6, s[12:13] offset:3072 nt
	v_add_u32_e32 v6, 0x8000, v6
	global_load_dwordx4 v[144:147], v6, s[12:13] offset:0 nt
	global_load_dwordx4 v[148:151], v6, s[12:13] offset:1024 nt
	global_load_dwordx4 v[152:155], v6, s[12:13] offset:2048 nt
	global_load_dwordx4 v[156:159], v6, s[12:13] offset:3072 nt
	s_and_b32 s6, s4, 3
	s_lshr_b32 s7, s4, 2
	v_and_b32_e32 v3, 15, v0
	v_bfe_u32 v7, v0, 4, 2
	v_and_b32_e32 v16, 1, v0
	v_cmp_eq_u32_e64 s[30:31], 0, v16
	v_and_b32_e32 v17, 2, v0
	v_cmp_eq_u32_e64 s[32:33], 0, v17
	v_and_b32_e32 v16, 3, v0
	v_lshrrev_b32_e32 v17, 2, v1
	v_lshlrev_b32_e32 v16, 5, v16
	v_lshl_add_u32 v16, v17, 1, v16
	v_lshrrev_b32_e32 v17, 1, v2
	s_movk_i32 s10, 0x110
	v_mad_u32_u24 v16, v17, s10, v16
	v_and_b32_e32 v17, 1, v2
	v_lshl_add_u32 v14, v17, 7, v16
	v_lshlrev_b32_e32 v17, 4, v7
	v_mad_u32_u24 v15, v3, s10, v17
	s_lshl_b32 s11, s6, 5
	v_lshl_add_u32 v18, v7, 2, s11
	v_cvt_f32_u32_e32 v18, v18
	v_lshlrev_b32_e32 v19, 3, v7
	v_cvt_f32_u32_e32 v19, v19
	s_waitcnt vmcnt(8)
	v_lshlrev_b32_e32 v16, 2, v3
	v_add_u32_e32 v17, 64, v16
	ds_bpermute_b32 v40, v16, v32
	ds_bpermute_b32 v46, v17, v32
	ds_bpermute_b32 v41, v16, v33
	ds_bpermute_b32 v47, v17, v33
	ds_bpermute_b32 v42, v16, v34
	ds_bpermute_b32 v48, v17, v34
	ds_bpermute_b32 v43, v16, v35
	ds_bpermute_b32 v49, v17, v35
	ds_bpermute_b32 v44, v16, v36
	ds_bpermute_b32 v50, v17, v36
	ds_bpermute_b32 v45, v16, v37
	ds_bpermute_b32 v51, v17, v37
	s_waitcnt lgkmcnt(0)
	v_add_f32_e32 v41, v40, v41
	v_sub_f32_e32 v12, v19, v42
	v_sub_f32_e32 v13, v18, v43
	v_rcp_f32_e32 v42, v40
	v_rcp_f32_e32 v43, v41
	s_nop 0
	v_fma_f32 v20, -v40, v42, 1.0
	v_fma_f32 v42, v20, v42, v42
	v_fma_f32 v20, -v41, v43, 1.0
	v_fma_f32 v43, v20, v43, v43
	v_mul_f32_e32 v8, 0xbf38aa3b, v42
	v_mul_f32_e32 v9, 0xbf38aa3b, v43
	v_mul_f32_e32 v44, v44, v42
	v_mul_f32_e32 v45, v45, v43
	v_mul_f32_e32 v10, 0x3e22f983, v44
	v_mul_f32_e32 v11, 0x3e22f983, v45
	v_add_f32_e32 v47, v46, v47
	v_sub_f32_e32 v2, v19, v48
	v_sub_f32_e32 v3, v18, v49
	v_rcp_f32_e32 v48, v46
	v_rcp_f32_e32 v49, v47
	s_nop 0
	v_fma_f32 v20, -v46, v48, 1.0
	v_fma_f32 v48, v20, v48, v48
	v_fma_f32 v20, -v47, v49, 1.0
	v_fma_f32 v49, v20, v49, v49
	v_mul_f32_e32 v28, 0xbf38aa3b, v48
	v_mul_f32_e32 v29, 0xbf38aa3b, v49
	v_mul_f32_e32 v50, v50, v48
	v_mul_f32_e32 v51, v51, v49
	v_mul_f32_e32 v30, 0x3e22f983, v50
	v_mul_f32_e32 v31, 0x3e22f983, v51
	s_getpc_b64 s[44:45]
